# V-transpose prep loops (both layers): all source loads of a unit issued up front instead of 4-at-a-time with full waits; first grid barrier census: 16 counter loads issued together
# speedup vs baseline: 1.0121x; 1.0058x over previous
; __device__ __forceinline__ unsigned xb_ld(unsigned* p)              { return __hip_atomic_load(p, __ATOMIC_RELAXED, __HIP_MEMORY_SCOPE_AGENT); }
; __device__ __forceinline__ void xcd_barrier_complete(unsigned* bar, unsigned x, unsigned& nloc, unsigned& nx) {
;     const unsigned G = gridDim.x * gridDim.y * gridDim.z;
;     unsigned sum, cnt, mine, sp = 0u;
;     for (;;) {
;         sum = 0u; cnt = 0u; mine = 0u;
; #pragma unroll
;         for (unsigned j = 0; j < 16; ++j) { const unsigned c = xb_ld(&bar[XB_XCNT(j)]); sum += c; cnt += (c > 0u) ? 1u : 0u; mine = (j == x) ? c : mine; }
;         if (sum == G) break;
;         __builtin_amdgcn_s_sleep(1);
;         if ((++sp & 255u) == 0u) { if (xb_ld(&bar[XB_TMO])) break; if (sp > XB_SPIN_CAP) { atomicAdd(&bar[XB_TMO], 1u); break; } }
;     }
.LBB0_30:
	s_mov_b64 s[6:7], -1
	global_load_dword v0, v233, s[70:71] sc1
	global_load_dword v1, v233, s[70:71] offset:256 sc1
	global_load_dword v2, v233, s[70:71] offset:512 sc1
	global_load_dword v3, v233, s[70:71] offset:768 sc1
	global_load_dword v4, v233, s[70:71] offset:1024 sc1
	global_load_dword v5, v233, s[70:71] offset:1280 sc1
	global_load_dword v6, v233, s[70:71] offset:1536 sc1
	global_load_dword v7, v233, s[70:71] offset:1792 sc1
	global_load_dword v8, v233, s[70:71] offset:2048 sc1
	global_load_dword v9, v233, s[70:71] offset:2304 sc1
	global_load_dword v10, v233, s[70:71] offset:2560 sc1
	global_load_dword v11, v233, s[70:71] offset:2816 sc1
	global_load_dword v12, v233, s[70:71] offset:3072 sc1
	global_load_dword v13, v233, s[70:71] offset:3328 sc1
	global_load_dword v14, v233, s[70:71] offset:3584 sc1
	global_load_dword v15, v233, s[70:71] offset:3840 sc1
	s_mov_b64 s[2:3], -1
	s_waitcnt vmcnt(0)
	v_add_u32_e32 v16, v1, v0
	v_add_u32_e32 v16, v16, v2
	v_add_u32_e32 v16, v16, v3
	v_add_u32_e32 v16, v16, v4
	v_add_u32_e32 v16, v16, v5
	v_add_u32_e32 v16, v16, v6
	v_add_u32_e32 v16, v16, v7
	v_add_u32_e32 v16, v16, v8
	v_add_u32_e32 v16, v16, v9
	v_add_u32_e32 v16, v16, v10
	v_add_u32_e32 v16, v16, v11
	v_add_u32_e32 v16, v16, v12
	v_add_u32_e32 v16, v16, v13
	v_add_u32_e32 v16, v16, v14
	v_add_u32_e32 v16, v16, v15
	v_cmp_eq_u32_e32 vcc, s15, v16
	s_cbranch_vccnz .LBB0_29
	s_and_b32 s2, s23, 0xff
	s_cmp_eq_u32 s2, 0
	s_mov_b64 s[2:3], -1
	s_mov_b64 s[8:9], -1
	s_sleep 1
	s_cbranch_scc1 .LBB0_34
	s_and_b64 vcc, exec, s[8:9]
	s_cbranch_vccz .LBB0_29

; template <bool DIL>
; __device__ __forceinline__ void phase_vt_heads(const unsigned char* V8, unsigned char* Vt1, unsigned char* Vt4, unsigned char* Vt16, LAS unsigned char* lds, int G, int bid, int tid) {
;     constexpr int PITCH = 272, IMG = 128 * PITCH;
;     const int cb = tid & 31, tq = tid >> 5;
;     for (int u = bid; u < 1024; u += G) {
;         const int b = u >> 7, h = (u >> 4) & 7, ch = u & 15;
;         const unsigned char* src = V8 + (size_t)(b * SEQ + 256 * ch) * 1024 + h * 128 + 4 * cb;
;         __syncthreads();
; #pragma unroll
;         for (int k = 0; k < 4; ++k) { const int tg = tq + 16 * k;
;             unsigned o[4];
;             { const int t0 = 4 * tg;
;               tr4x4(*(const unsigned*)(src + (size_t)(t0 + 0) * 1024), *(const unsigned*)(src + (size_t)(t0 + 1) * 1024), *(const unsigned*)(src + (size_t)(t0 + 2) * 1024), *(const unsigned*)(src + (size_t)(t0 + 3) * 1024), o);
; #pragma unroll
;               for (int j = 0; j < 4; ++j) *(LAS unsigned*)(lds + (4 * cb + j) * PITCH + 4 * tg) = o[j]; }
;             if constexpr (DIL) {
;                 { const int r = tg & 3, g = tg >> 2; const int t0 = r + 16 * g;
;                   tr4x4(*(const unsigned*)(src + (size_t)(t0 + 0) * 1024), *(const unsigned*)(src + (size_t)(t0 + 4) * 1024), *(const unsigned*)(src + (size_t)(t0 + 8) * 1024), *(const unsigned*)(src + (size_t)(t0 + 12) * 1024), o);
; #pragma unroll
;                   for (int j = 0; j < 4; ++j) *(LAS unsigned*)(lds + IMG + (4 * cb + j) * PITCH + r * 64 + 4 * g) = o[j]; }
;                 { const int cls = tg & 15, g = tg >> 4; const int t0 = cls + 64 * g;
;                   tr4x4(*(const unsigned*)(src + (size_t)(t0 + 0) * 1024), *(const unsigned*)(src + (size_t)(t0 + 16) * 1024), *(const unsigned*)(src + (size_t)(t0 + 32) * 1024), *(const unsigned*)(src + (size_t)(t0 + 48) * 1024), o);
; #pragma unroll
;                   for (int j = 0; j < 4; ++j) *(LAS unsigned*)(lds + 2 * IMG + (4 * cb + j) * PITCH + cls * 16 + 4 * g) = o[j]; }
;             }
;         }
;         __syncthreads();
;         const size_t cbase = (size_t)(b * 8 + h) * 128;
; #pragma unroll
;         for (int k = 0; k < 4; ++k) { const int id = tid + NTHR * k, col = id >> 4, pc = id & 15;
;             *(u32x4*)(Vt1 + (cbase + col) * SEQ + 256 * ch + pc * 16) = *(const LAS u32x4*)(lds + col * PITCH + pc * 16);
.LBB0_227:
	s_ashr_i32 s23, s9, 7
	s_lshl_b32 s25, s23, 12
	s_and_b32 s15, s8, 0xf00
	s_or_b32 s28, s25, s15
	s_ashr_i32 s29, s28, 31
	s_bfe_u32 s24, s9, 0x30004
	s_lshl_b64 s[28:29], s[28:29], 10
	s_add_u32 s25, s0, s28
	s_addc_u32 s29, s1, s29
	s_lshl_b32 s28, s24, 7
	s_add_u32 s28, s25, s28
	s_addc_u32 s29, s29, 0
	v_lshl_add_u64 v[42:43], s[28:29], 0, v[232:233]
	s_waitcnt vmcnt(0)
	v_lshl_add_u64 v[50:51], v[42:43], 0, v[2:3]
	global_load_dword v176, v[50:51], off
	v_lshl_add_u64 v[50:51], v[42:43], 0, v[4:5]
	global_load_dword v177, v[50:51], off
	v_lshl_add_u64 v[50:51], v[42:43], 0, v[6:7]
	global_load_dword v178, v[50:51], off
	v_lshl_add_u64 v[50:51], v[42:43], 0, v[8:9]
	global_load_dword v179, v[50:51], off
	v_lshl_add_u64 v[50:51], v[42:43], 0, v[10:11]
	global_load_dword v180, v[50:51], off
	v_lshl_add_u64 v[50:51], v[42:43], 0, v[12:13]
	global_load_dword v181, v[50:51], off
	v_lshl_add_u64 v[50:51], v[42:43], 0, v[14:15]
	global_load_dword v182, v[50:51], off
	v_lshl_add_u64 v[50:51], v[42:43], 0, v[16:17]
	global_load_dword v183, v[50:51], off
	v_lshl_add_u64 v[50:51], v[42:43], 0, v[18:19]
	global_load_dword v184, v[50:51], off
	v_lshl_add_u64 v[50:51], v[42:43], 0, v[20:21]
	global_load_dword v185, v[50:51], off
	v_lshl_add_u64 v[50:51], v[42:43], 0, v[22:23]
	global_load_dword v186, v[50:51], off
	v_lshl_add_u64 v[50:51], v[42:43], 0, v[24:25]
	global_load_dword v187, v[50:51], off
	v_lshl_add_u64 v[50:51], v[42:43], 0, v[26:27]
	global_load_dword v188, v[50:51], off
	v_lshl_add_u64 v[50:51], v[42:43], 0, v[28:29]
	global_load_dword v189, v[50:51], off
	v_lshl_add_u64 v[50:51], v[42:43], 0, v[30:31]
	global_load_dword v190, v[50:51], off
	v_lshl_add_u64 v[50:51], v[42:43], 0, v[32:33]
	global_load_dword v191, v[50:51], off
	s_barrier
	s_lshl_b32 s23, s23, 3
	s_or_b32 s24, s23, s24
	s_ashr_i32 s25, s24, 31
	s_lshl_b64 s[24:25], s[24:25], 19
	s_add_u32 s23, s6, s24
	s_addc_u32 s25, s7, s25
	s_add_u32 s24, s23, s15
	s_addc_u32 s25, s25, 0
	s_add_i32 s9, s9, s50
	s_add_i32 s8, s8, s49
	s_cmpk_lt_i32 s9, 0x400
	s_waitcnt vmcnt(14)
	v_perm_b32 v51, v177, v176, s82
	v_perm_b32 v49, v177, v176, s88
	s_waitcnt vmcnt(12)
	v_perm_b32 v52, v179, v178, s82
	v_perm_b32 v50, v179, v178, s88
	v_perm_b32 v53, v52, v51, s13
	v_perm_b32 v52, v52, v51, s17
	v_perm_b32 v54, v50, v49, s13
	v_perm_b32 v49, v50, v49, s17
	s_waitcnt vmcnt(10)
	v_perm_b32 v51, v181, v180, s82
	v_perm_b32 v55, v181, v180, s88
	s_waitcnt vmcnt(8)
	v_perm_b32 v56, v183, v182, s82
	v_perm_b32 v50, v183, v182, s88
	v_perm_b32 v57, v56, v51, s13
	v_perm_b32 v51, v56, v51, s17
	v_perm_b32 v56, v50, v55, s13
	v_perm_b32 v50, v50, v55, s17
	ds_write2_b32 v44, v53, v57 offset1:16
	ds_write2_b32 v44, v52, v51 offset0:68 offset1:84
	ds_write2_b32 v44, v54, v56 offset0:136 offset1:152
	ds_write2_b32 v44, v49, v50 offset0:204 offset1:220
	s_waitcnt vmcnt(6)
	v_perm_b32 v51, v185, v184, s82
	v_perm_b32 v49, v185, v184, s88
	s_waitcnt vmcnt(4)
	v_perm_b32 v52, v187, v186, s82
	v_perm_b32 v50, v187, v186, s88
	v_perm_b32 v53, v52, v51, s13
	v_perm_b32 v52, v52, v51, s17
	v_perm_b32 v54, v50, v49, s13
	v_perm_b32 v49, v50, v49, s17
	s_waitcnt vmcnt(2)
	v_perm_b32 v43, v189, v188, s82
	v_perm_b32 v51, v189, v188, s88
	s_waitcnt vmcnt(0)
	v_perm_b32 v55, v191, v190, s82
	v_perm_b32 v42, v191, v190, s88
	v_perm_b32 v50, v55, v43, s13
	v_perm_b32 v43, v55, v43, s17
	v_perm_b32 v55, v42, v51, s13
	v_perm_b32 v42, v42, v51, s17
	ds_write2_b32 v44, v53, v50 offset0:32 offset1:48
	ds_write2_b32 v44, v52, v43 offset0:100 offset1:116
	ds_write2_b32 v44, v54, v55 offset0:168 offset1:184
	ds_write2_b32 v44, v49, v42 offset0:236 offset1:252
	s_waitcnt lgkmcnt(0)
	s_barrier
	ds_read_b128 v[50:53], v45
	v_lshl_add_u64 v[42:43], s[24:25], 0, v[0:1]
	v_lshl_add_u64 v[54:55], v[42:43], 0, v[34:35]
	s_waitcnt lgkmcnt(0)
	global_store_dwordx4 v[54:55], v[50:53], off
	ds_read_b128 v[50:53], v46
	v_lshl_add_u64 v[54:55], v[42:43], 0, v[36:37]
	s_waitcnt lgkmcnt(0)
	global_store_dwordx4 v[54:55], v[50:53], off
	ds_read_b128 v[50:53], v47
	v_lshl_add_u64 v[54:55], v[42:43], 0, v[38:39]
	v_lshl_add_u64 v[42:43], v[42:43], 0, v[40:41]
	s_waitcnt lgkmcnt(0)
	global_store_dwordx4 v[54:55], v[50:53], off
	ds_read_b128 v[50:53], v48
	s_waitcnt lgkmcnt(0)
	global_store_dwordx4 v[42:43], v[50:53], off
	s_cbranch_scc1 .LBB0_227

; #define LAS __attribute__((address_space(3)))
; template <bool DIL>
; __device__ __forceinline__ void phase_vt_heads(const unsigned char* V8, unsigned char* Vt1, unsigned char* Vt4, unsigned char* Vt16, LAS unsigned char* lds, int G, int bid, int tid) {
;     ...
;     for (int u = bid; u < 1024; u += G) {
;         const int b = u >> 7, h = (u >> 4) & 7, ch = u & 15;
;         const unsigned char* src = V8 + (size_t)(b * SEQ + 256 * ch) * 1024 + h * 128 + 4 * cb;
;         __syncthreads();
; #pragma unroll
;         for (int k = 0; k < 4; ++k) { const int tg = tq + 16 * k;
;             unsigned o[4];
;             { const int t0 = 4 * tg;
;               tr4x4(*(const unsigned*)(src + (size_t)(t0 + 0) * 1024), *(const unsigned*)(src + (size_t)(t0 + 1) * 1024), *(const unsigned*)(src + (size_t)(t0 + 2) * 1024), *(const unsigned*)(src + (size_t)(t0 + 3) * 1024), o);
; #pragma unroll
;               for (int j = 0; j < 4; ++j) *(LAS unsigned*)(lds + (4 * cb + j) * PITCH + 4 * tg) = o[j]; }
;             if constexpr (DIL) {
;                 { const int r = tg & 3, g = tg >> 2; const int t0 = r + 16 * g;
;                   tr4x4(*(const unsigned*)(src + (size_t)(t0 + 0) * 1024), *(const unsigned*)(src + (size_t)(t0 + 4) * 1024), *(const unsigned*)(src + (size_t)(t0 + 8) * 1024), *(const unsigned*)(src + (size_t)(t0 + 12) * 1024), o);
; #pragma unroll
;                   for (int j = 0; j < 4; ++j) *(LAS unsigned*)(lds + IMG + (4 * cb + j) * PITCH + r * 64 + 4 * g) = o[j]; }
;                 { const int cls = tg & 15, g = tg >> 4; const int t0 = cls + 64 * g;
;                   tr4x4(*(const unsigned*)(src + (size_t)(t0 + 0) * 1024), *(const unsigned*)(src + (size_t)(t0 + 16) * 1024), *(const unsigned*)(src + (size_t)(t0 + 32) * 1024), *(const unsigned*)(src + (size_t)(t0 + 48) * 1024), o);
; #pragma unroll
;                   for (int j = 0; j < 4; ++j) *(LAS unsigned*)(lds + 2 * IMG + (4 * cb + j) * PITCH + cls * 16 + 4 * g) = o[j]; }
;             }
;         }
;         __syncthreads();
.LBB0_247:
	s_ashr_i32 s0, s2, 7
	s_and_b32 s3, s2, 15
	s_lshl_b32 s8, s0, 12
	s_lshl_b32 s36, s3, 8
	s_or_b32 s8, s8, s36
	s_ashr_i32 s9, s8, 31
	s_bfe_u32 s1, s2, 0x30004
	s_lshl_b64 s[8:9], s[8:9], 10
	s_add_u32 s8, s6, s8
	s_addc_u32 s9, s7, s9
	s_lshl_b32 s15, s1, 7
	s_add_u32 s8, s8, s15
	s_addc_u32 s9, s9, 0
	v_lshl_add_u64 v[110:111], s[8:9], 0, v[232:233]
	v_lshl_add_u64 v[112:113], v[110:111], 0, v[6:7]
	global_load_dword v176, v[112:113], off
	v_lshl_add_u64 v[112:113], v[110:111], 0, v[8:9]
	global_load_dword v177, v[112:113], off
	v_lshl_add_u64 v[112:113], v[110:111], 0, v[10:11]
	global_load_dword v178, v[112:113], off
	v_lshl_add_u64 v[112:113], v[110:111], 0, v[12:13]
	global_load_dword v179, v[112:113], off
	v_lshl_add_u64 v[112:113], v[110:111], 0, v[14:15]
	global_load_dword v180, v[112:113], off
	v_lshl_add_u64 v[112:113], v[110:111], 0, v[16:17]
	global_load_dword v181, v[112:113], off
	v_lshl_add_u64 v[112:113], v[110:111], 0, v[18:19]
	global_load_dword v182, v[112:113], off
	v_lshl_add_u64 v[112:113], v[110:111], 0, v[20:21]
	global_load_dword v183, v[112:113], off
	v_lshl_add_u64 v[112:113], v[110:111], 0, v[22:23]
	global_load_dword v184, v[112:113], off
	v_lshl_add_u64 v[112:113], v[110:111], 0, v[24:25]
	global_load_dword v185, v[112:113], off
	v_lshl_add_u64 v[112:113], v[110:111], 0, v[26:27]
	global_load_dword v186, v[112:113], off
	v_lshl_add_u64 v[112:113], v[110:111], 0, v[28:29]
	global_load_dword v187, v[112:113], off
	v_lshl_add_u64 v[112:113], v[110:111], 0, v[30:31]
	global_load_dword v188, v[112:113], off
	v_lshl_add_u64 v[112:113], v[110:111], 0, v[32:33]
	global_load_dword v189, v[112:113], off
	v_lshl_add_u64 v[112:113], v[110:111], 0, v[34:35]
	global_load_dword v190, v[112:113], off
	v_lshl_add_u64 v[112:113], v[110:111], 0, v[36:37]
	global_load_dword v191, v[112:113], off
	v_lshl_add_u64 v[112:113], v[110:111], 0, v[38:39]
	global_load_dword v192, v[112:113], off
	v_lshl_add_u64 v[112:113], v[110:111], 0, v[40:41]
	global_load_dword v193, v[112:113], off
	v_lshl_add_u64 v[112:113], v[110:111], 0, v[42:43]
	global_load_dword v194, v[112:113], off
	v_lshl_add_u64 v[112:113], v[110:111], 0, v[44:45]
	global_load_dword v195, v[112:113], off
	v_lshl_add_u64 v[112:113], v[110:111], 0, v[46:47]
	global_load_dword v196, v[112:113], off
	v_lshl_add_u64 v[112:113], v[110:111], 0, v[48:49]
	global_load_dword v197, v[112:113], off
	v_lshl_add_u64 v[112:113], v[110:111], 0, v[50:51]
	global_load_dword v198, v[112:113], off
	v_lshl_add_u64 v[112:113], v[110:111], 0, v[52:53]
	global_load_dword v199, v[112:113], off
	v_lshl_add_u64 v[112:113], v[110:111], 0, v[54:55]
	global_load_dword v200, v[112:113], off
	v_lshl_add_u64 v[112:113], v[110:111], 0, v[56:57]
	global_load_dword v201, v[112:113], off
	v_lshl_add_u64 v[112:113], v[110:111], 0, v[58:59]
	global_load_dword v202, v[112:113], off
	v_lshl_add_u64 v[112:113], v[110:111], 0, v[60:61]
	global_load_dword v203, v[112:113], off
	v_lshl_add_u64 v[112:113], v[110:111], 0, v[62:63]
	global_load_dword v209, v[112:113], off
	v_lshl_add_u64 v[112:113], v[110:111], 0, v[64:65]
	global_load_dword v210, v[112:113], off
	v_lshl_add_u64 v[112:113], v[110:111], 0, v[66:67]
	global_load_dword v211, v[112:113], off
	v_lshl_add_u64 v[112:113], v[110:111], 0, v[68:69]
	global_load_dword v212, v[112:113], off
	v_lshl_add_u64 v[112:113], v[110:111], 0, v[70:71]
	global_load_dword v213, v[112:113], off
	v_lshl_add_u64 v[112:113], v[110:111], 0, v[72:73]
	global_load_dword v214, v[112:113], off
	v_lshl_add_u64 v[112:113], v[110:111], 0, v[74:75]
	global_load_dword v215, v[112:113], off
	v_lshl_add_u64 v[112:113], v[110:111], 0, v[76:77]
	global_load_dword v218, v[112:113], off
	v_lshl_add_u64 v[112:113], v[110:111], 0, v[78:79]
	global_load_dword v219, v[112:113], off
	v_lshl_add_u64 v[112:113], v[110:111], 0, v[80:81]
	global_load_dword v220, v[112:113], off
	v_lshl_add_u64 v[112:113], v[110:111], 0, v[82:83]
	global_load_dword v221, v[112:113], off
	v_lshl_add_u64 v[112:113], v[110:111], 0, v[84:85]
	global_load_dword v222, v[112:113], off
	v_lshl_add_u64 v[112:113], v[110:111], 0, v[86:87]
	global_load_dword v223, v[112:113], off
	v_lshl_add_u64 v[112:113], v[110:111], 0, v[88:89]
	global_load_dword v224, v[112:113], off
	v_lshl_add_u64 v[112:113], v[110:111], 0, v[90:91]
	global_load_dword v225, v[112:113], off
	v_lshl_add_u64 v[112:113], v[110:111], 0, v[92:93]
	global_load_dword v226, v[112:113], off
	v_lshl_add_u64 v[112:113], v[110:111], 0, v[94:95]
	global_load_dword v227, v[112:113], off
	v_lshl_add_u64 v[112:113], v[110:111], 0, v[96:97]
	global_load_dword v229, v[112:113], off
	v_lshl_add_u64 v[112:113], v[110:111], 0, v[98:99]
	global_load_dword v230, v[112:113], off
	v_lshl_add_u64 v[112:113], v[110:111], 0, v[100:101]
	global_load_dword v231, v[112:113], off
	s_barrier
; #define LAS __attribute__((address_space(3)))
; template <bool DIL>
; __device__ __forceinline__ void phase_vt_heads(const unsigned char* V8, unsigned char* Vt1, unsigned char* Vt4, unsigned char* Vt16, LAS unsigned char* lds, int G, int bid, int tid) {
;     ...
;     for (int u = bid; u < 1024; u += G) {
;         const int b = u >> 7, h = (u >> 4) & 7, ch = u & 15;
;         const unsigned char* src = V8 + (size_t)(b * SEQ + 256 * ch) * 1024 + h * 128 + 4 * cb;
;         __syncthreads();
; #pragma unroll
;         for (int k = 0; k < 4; ++k) { const int tg = tq + 16 * k;
;             unsigned o[4];
;             { const int t0 = 4 * tg;
;               tr4x4(*(const unsigned*)(src + (size_t)(t0 + 0) * 1024), *(const unsigned*)(src + (size_t)(t0 + 1) * 1024), *(const unsigned*)(src + (size_t)(t0 + 2) * 1024), *(const unsigned*)(src + (size_t)(t0 + 3) * 1024), o);
; #pragma unroll
;               for (int j = 0; j < 4; ++j) *(LAS unsigned*)(lds + (4 * cb + j) * PITCH + 4 * tg) = o[j]; }
;             if constexpr (DIL) {
;                 { const int r = tg & 3, g = tg >> 2; const int t0 = r + 16 * g;
;                   tr4x4(*(const unsigned*)(src + (size_t)(t0 + 0) * 1024), *(const unsigned*)(src + (size_t)(t0 + 4) * 1024), *(const unsigned*)(src + (size_t)(t0 + 8) * 1024), *(const unsigned*)(src + (size_t)(t0 + 12) * 1024), o);
; #pragma unroll
;                   for (int j = 0; j < 4; ++j) *(LAS unsigned*)(lds + IMG + (4 * cb + j) * PITCH + r * 64 + 4 * g) = o[j]; }
;                 { const int cls = tg & 15, g = tg >> 4; const int t0 = cls + 64 * g;
;                   tr4x4(*(const unsigned*)(src + (size_t)(t0 + 0) * 1024), *(const unsigned*)(src + (size_t)(t0 + 16) * 1024), *(const unsigned*)(src + (size_t)(t0 + 32) * 1024), *(const unsigned*)(src + (size_t)(t0 + 48) * 1024), o);
; #pragma unroll
;                   for (int j = 0; j < 4; ++j) *(LAS unsigned*)(lds + 2 * IMG + (4 * cb + j) * PITCH + cls * 16 + 4 * g) = o[j]; }
;             }
;         }
	s_lshl_b32 s0, s0, 3
	v_add_u32_e32 v142, v116, v118
	s_or_b32 s0, s0, s1
	s_ashr_i32 s1, s0, 31
	s_lshl_b64 s[0:1], s[0:1], 19
	v_lshl_add_u64 v[138:139], s[0:1], 0, v[102:103]
	s_add_i32 s2, s2, s50
	s_waitcnt vmcnt(46)
	v_perm_b32 v113, v177, v176, s82
	v_perm_b32 v114, v177, v176, s88
	s_waitcnt vmcnt(44)
	v_perm_b32 v115, v179, v178, s82
	v_perm_b32 v112, v179, v178, s88
	v_perm_b32 v134, v115, v113, s13
	v_perm_b32 v113, v115, v113, s17
	v_perm_b32 v115, v112, v114, s13
	v_perm_b32 v112, v112, v114, s17
	ds_write2_b32 v122, v134, v113 offset1:68
	ds_write2_b32 v122, v115, v112 offset0:136 offset1:204
	s_waitcnt vmcnt(42)
	v_perm_b32 v113, v181, v180, s82
	v_perm_b32 v114, v181, v180, s88
	s_waitcnt vmcnt(40)
	v_perm_b32 v115, v183, v182, s82
	v_perm_b32 v112, v183, v182, s88
	v_perm_b32 v134, v115, v113, s13
	v_perm_b32 v113, v115, v113, s17
	v_perm_b32 v115, v112, v114, s13
	v_perm_b32 v112, v112, v114, s17
	v_add_u32_e32 v114, 0x8800, v123
	ds_write2_b32 v114, v134, v113 offset1:68
	ds_write2_b32 v114, v115, v112 offset0:136 offset1:204
	s_waitcnt vmcnt(38)
	v_perm_b32 v113, v185, v184, s82
	v_perm_b32 v114, v185, v184, s88
	s_waitcnt vmcnt(36)
	v_perm_b32 v115, v187, v186, s82
	v_perm_b32 v112, v187, v186, s88
	v_perm_b32 v134, v115, v113, s13
	v_perm_b32 v113, v115, v113, s17
	v_perm_b32 v115, v112, v114, s13
	v_perm_b32 v112, v112, v114, s17
	ds_write2_b32 v124, v134, v113 offset1:68
	ds_write2_b32 v124, v115, v112 offset0:136 offset1:204
	s_waitcnt vmcnt(34)
	v_perm_b32 v113, v189, v188, s82
	v_perm_b32 v114, v189, v188, s88
	s_waitcnt vmcnt(32)
	v_perm_b32 v115, v191, v190, s82
	v_perm_b32 v112, v191, v190, s88
	v_perm_b32 v134, v115, v113, s13
	v_perm_b32 v113, v115, v113, s17
	v_perm_b32 v115, v112, v114, s13
	v_perm_b32 v112, v112, v114, s17
	ds_write2_b32 v125, v134, v113 offset1:68
	ds_write2_b32 v125, v115, v112 offset0:136 offset1:204
	s_waitcnt vmcnt(30)
	v_perm_b32 v113, v193, v192, s82
	v_perm_b32 v114, v193, v192, s88
	s_waitcnt vmcnt(28)
	v_perm_b32 v115, v195, v194, s82
	v_perm_b32 v112, v195, v194, s88
	v_perm_b32 v134, v115, v113, s13
	v_perm_b32 v113, v115, v113, s17
	v_perm_b32 v115, v112, v114, s13
	v_perm_b32 v112, v112, v114, s17
	v_add_u32_e32 v114, 0x8800, v126
	ds_write2_b32 v114, v134, v113 offset1:68
	ds_write2_b32 v114, v115, v112 offset0:136 offset1:204
	s_waitcnt vmcnt(26)
	v_perm_b32 v113, v197, v196, s82
	v_perm_b32 v114, v197, v196, s88
	s_waitcnt vmcnt(24)
	v_perm_b32 v115, v199, v198, s82
	v_perm_b32 v112, v199, v198, s88
	v_perm_b32 v134, v115, v113, s13
	v_perm_b32 v113, v115, v113, s17
	v_perm_b32 v115, v112, v114, s13
	v_perm_b32 v112, v112, v114, s17
	ds_write2_b32 v127, v134, v113 offset1:68
	ds_write2_b32 v127, v115, v112 offset0:136 offset1:204
	s_waitcnt vmcnt(22)
	v_perm_b32 v113, v201, v200, s82
	v_perm_b32 v114, v201, v200, s88
	s_waitcnt vmcnt(20)
	v_perm_b32 v115, v203, v202, s82
	v_perm_b32 v112, v203, v202, s88
	v_perm_b32 v134, v115, v113, s13
	v_perm_b32 v113, v115, v113, s17
	v_perm_b32 v115, v112, v114, s13
	v_perm_b32 v112, v112, v114, s17
	ds_write2_b32 v128, v134, v113 offset1:68
	ds_write2_b32 v128, v115, v112 offset0:136 offset1:204
	s_waitcnt vmcnt(18)
	v_perm_b32 v113, v210, v209, s82
	v_perm_b32 v114, v210, v209, s88
	s_waitcnt vmcnt(16)
	v_perm_b32 v115, v212, v211, s82
	v_perm_b32 v112, v212, v211, s88
	v_perm_b32 v134, v115, v113, s13
	v_perm_b32 v113, v115, v113, s17
	v_perm_b32 v115, v112, v114, s13
	v_perm_b32 v112, v112, v114, s17
	v_add_u32_e32 v114, 0x8800, v129
	ds_write2_b32 v114, v134, v113 offset1:68
	ds_write2_b32 v114, v115, v112 offset0:136 offset1:204
	s_waitcnt vmcnt(14)
	v_perm_b32 v113, v214, v213, s82
	v_perm_b32 v114, v214, v213, s88
	s_waitcnt vmcnt(12)
	v_perm_b32 v115, v218, v215, s82
	v_perm_b32 v112, v218, v215, s88
	v_perm_b32 v134, v115, v113, s13
	v_perm_b32 v113, v115, v113, s17
	v_perm_b32 v115, v112, v114, s13
	v_perm_b32 v112, v112, v114, s17
	ds_write2_b32 v130, v134, v113 offset1:68
	ds_write2_b32 v130, v115, v112 offset0:136 offset1:204
	s_waitcnt vmcnt(10)
	v_perm_b32 v113, v220, v219, s82
	v_perm_b32 v114, v220, v219, s88
	s_waitcnt vmcnt(8)
	v_perm_b32 v115, v222, v221, s82
	v_perm_b32 v112, v222, v221, s88
	v_perm_b32 v134, v115, v113, s13
	v_perm_b32 v113, v115, v113, s17
	v_perm_b32 v115, v112, v114, s13
	v_perm_b32 v112, v112, v114, s17
	ds_write2_b32 v131, v134, v113 offset1:68
	ds_write2_b32 v131, v115, v112 offset0:136 offset1:204
	s_waitcnt vmcnt(6)
	v_perm_b32 v113, v224, v223, s82
	v_perm_b32 v114, v224, v223, s88
	s_waitcnt vmcnt(4)
	v_perm_b32 v115, v226, v225, s82
	v_perm_b32 v112, v226, v225, s88
	v_perm_b32 v134, v115, v113, s13
	v_perm_b32 v113, v115, v113, s17
	v_perm_b32 v115, v112, v114, s13
	v_perm_b32 v112, v112, v114, s17
	v_add_u32_e32 v114, 0x8800, v132
	ds_write2_b32 v114, v134, v113 offset1:68
	ds_write2_b32 v114, v115, v112 offset0:136 offset1:204
	s_waitcnt vmcnt(2)
	v_perm_b32 v111, v229, v227, s82
	v_perm_b32 v113, v229, v227, s88
	s_waitcnt vmcnt(0)
	v_perm_b32 v114, v231, v230, s82
	v_perm_b32 v110, v231, v230, s88
	v_perm_b32 v112, v114, v111, s13
	v_perm_b32 v111, v114, v111, s17
	v_perm_b32 v114, v110, v113, s13
	v_perm_b32 v110, v110, v113, s17
	ds_write2_b32 v133, v112, v111 offset1:68
	ds_write2_b32 v133, v114, v110 offset0:136 offset1:204
	s_waitcnt lgkmcnt(0)
	s_barrier
; #define LAS __attribute__((address_space(3)))
; template <bool DIL>
; __device__ __forceinline__ void phase_vt_heads(const unsigned char* V8, unsigned char* Vt1, unsigned char* Vt4, unsigned char* Vt16, LAS unsigned char* lds, int G, int bid, int tid) {
;     ...
;         __syncthreads();
;         const size_t cbase = (size_t)(b * 8 + h) * 128;
; #pragma unroll
;         for (int k = 0; k < 4; ++k) { const int id = tid + NTHR * k, col = id >> 4, pc = id & 15;
;             *(u32x4*)(Vt1 + (cbase + col) * SEQ + 256 * ch + pc * 16) = *(const LAS u32x4*)(lds + col * PITCH + pc * 16);
;             if constexpr (DIL) {
;                 *(u32x4*)(Vt4 + (cbase + col) * SEQ + (pc >> 2) * 1024 + 64 * ch + (pc & 3) * 16) = *(const LAS u32x4*)(lds + IMG + col * PITCH + pc * 16);
;                 *(u32x4*)(Vt16 + (cbase + col) * SEQ + pc * 256 + 16 * ch) = *(const LAS u32x4*)(lds + 2 * IMG + col * PITCH + pc * 16); } }
;     }
	ds_read_b128 v[134:137], v142
	v_lshl_add_u64 v[114:115], v[0:1], 0, s[36:37]
	v_lshl_add_u64 v[140:141], v[114:115], 0, v[138:139]
	s_lshl_b32 s36, s3, 6
	v_lshl_add_u64 v[112:113], v[2:3], 0, s[36:37]
	s_waitcnt lgkmcnt(0)
	global_store_dwordx4 v[140:141], v[134:137], off
	ds_read_b128 v[134:137], v142 offset:34816
	v_lshl_add_u64 v[140:141], v[112:113], 0, v[138:139]
	s_lshl_b32 s36, s3, 4
	v_lshl_add_u64 v[110:111], v[4:5], 0, s[36:37]
	v_lshl_add_u64 v[138:139], v[110:111], 0, v[138:139]
	s_waitcnt lgkmcnt(0)
	global_store_dwordx4 v[140:141], v[134:137], off
	v_add_u32_e32 v142, v116, v119
	s_cmpk_lt_i32 s2, 0x400
	v_add_u32_e32 v134, v117, v118
	ds_read_b128 v[134:137], v134
	s_waitcnt lgkmcnt(0)
	global_store_dwordx4 v[138:139], v[134:137], off
	ds_read_b128 v[134:137], v142
	v_lshl_add_u64 v[138:139], s[0:1], 0, v[104:105]
	v_lshl_add_u64 v[140:141], v[114:115], 0, v[138:139]
	s_waitcnt lgkmcnt(0)
	global_store_dwordx4 v[140:141], v[134:137], off
	ds_read_b128 v[134:137], v142 offset:34816
	v_lshl_add_u64 v[140:141], v[112:113], 0, v[138:139]
	v_lshl_add_u64 v[138:139], v[110:111], 0, v[138:139]
	v_add_u32_e32 v142, v116, v120
	s_waitcnt lgkmcnt(0)
	global_store_dwordx4 v[140:141], v[134:137], off
	s_nop 1
	v_add_u32_e32 v134, v117, v119
	ds_read_b128 v[134:137], v134
	s_waitcnt lgkmcnt(0)
	global_store_dwordx4 v[138:139], v[134:137], off
	ds_read_b128 v[134:137], v142
	v_lshl_add_u64 v[138:139], s[0:1], 0, v[106:107]
	v_lshl_add_u64 v[140:141], v[114:115], 0, v[138:139]
	s_waitcnt lgkmcnt(0)
	global_store_dwordx4 v[140:141], v[134:137], off
	ds_read_b128 v[134:137], v142 offset:34816
	v_lshl_add_u64 v[140:141], v[112:113], 0, v[138:139]
	v_lshl_add_u64 v[138:139], v[110:111], 0, v[138:139]
	s_waitcnt lgkmcnt(0)
	global_store_dwordx4 v[140:141], v[134:137], off
	s_nop 1
	v_add_u32_e32 v134, v117, v120
	ds_read_b128 v[134:137], v134
	v_add_u32_e32 v140, v116, v121
	s_waitcnt lgkmcnt(0)
	global_store_dwordx4 v[138:139], v[134:137], off
	ds_read_b128 v[134:137], v140
	v_lshl_add_u64 v[138:139], s[0:1], 0, v[108:109]
	v_lshl_add_u64 v[114:115], v[114:115], 0, v[138:139]
	v_lshl_add_u64 v[112:113], v[112:113], 0, v[138:139]
	v_lshl_add_u64 v[110:111], v[110:111], 0, v[138:139]
	s_waitcnt lgkmcnt(0)
	global_store_dwordx4 v[114:115], v[134:137], off
	ds_read_b128 v[134:137], v140 offset:34816
	s_waitcnt lgkmcnt(0)
	global_store_dwordx4 v[112:113], v[134:137], off
	v_add_u32_e32 v112, v117, v121
	ds_read_b128 v[112:115], v112
	s_waitcnt lgkmcnt(0)
	global_store_dwordx4 v[110:111], v[112:115], off
	s_cbranch_scc1 .LBB0_247
